# speedup vs baseline: 1.0182x; 1.0040x over previous
.LBB6_30:
	s_or_b64 exec, exec, s[4:5]
	s_load_dwordx2 s[8:9], s[0:1], 0x48
	s_waitcnt vmcnt(4)
	v_and_b32_e32 v2, 0x100, v0
	v_cmp_ne_u32_e64 s[0:1], 0, v2
	s_and_saveexec_b64 s[2:3], s[0:1]
	s_cbranch_execz .LBB6_32
	s_barrier

.LBB8_4:
	s_or_b64 exec, exec, s[4:5]
	s_load_dwordx2 s[8:9], s[0:1], 0x48
	s_waitcnt vmcnt(4)
	v_and_b32_e32 v1, 0x100, v0
	v_cmp_ne_u32_e64 s[0:1], 0, v1
	s_and_saveexec_b64 s[2:3], s[0:1]
	s_cbranch_execz .LBB8_6
	s_barrier
